# prologue row conversion: wave-wide sum via DPP and permlane swaps instead of six ds_bpermute round trips (bit-identical), on top of the grouped loads
# baseline (speedup 1.0000x reference)
; __device__ __forceinline__ unsigned pk2(float lo, float hi) { return f2bf(lo) | (f2bf(hi) << 16); }
; __device__ __forceinline__ float bf2f_lo(unsigned w) { return __uint_as_float(w << 16); }
; __device__ __forceinline__ float bf2f_hi(unsigned w) { return __uint_as_float(w & 0xffff0000u); }
; __device__ __forceinline__ float wave_sum(float v) {
; #pragma unroll
;     for (int o = 1; o < 64; o <<= 1) v += __shfl_xor(v, o);
;     return v;
; }
; __device__ __forceinline__ void p0_prologue(Frame& F, KArgs A) {
;     ...
;         for (int j = 0; j < 4; ++j) { const f32x4 v = xr[64 * j]; const unsigned a = pk2(v.x, v.y), b = pk2(v.z, v.w); o8[64 * j] = (unsigned long long)a | ((unsigned long long)b << 32);
;             s += (bf2f_lo(a) * bf2f_lo(a) + bf2f_hi(a) * bf2f_hi(a)) + (bf2f_lo(b) * bf2f_lo(b) + bf2f_hi(b) * bf2f_hi(b)); }
;         s = wave_sum(s);
.LBB0_355:
	s_add_i32 s8, s3, 0xffff8000
	s_cmpk_gt_i32 s3, 0x7fff
	s_cselect_b32 s9, 8, 0
	s_cselect_b32 s8, s8, s3
	s_cselect_b32 s22, s21, 0x7a00000
	s_add_u32 s10, s14, s9
	s_addc_u32 s11, s15, 0
	s_load_dwordx2 s[10:11], s[10:11], 0x0
	s_ashr_i32 s9, s8, 31
	s_lshl_b64 s[16:17], s[8:9], 12
	s_waitcnt lgkmcnt(0)
	s_add_u32 s16, s10, s16
	s_addc_u32 s17, s11, s17
	global_load_dwordx4 v[14:17], v13, s[16:17]
	global_load_dwordx4 v[32:35], v13, s[16:17] offset:1024
	global_load_dwordx4 v[36:39], v13, s[16:17] offset:2048
	global_load_dwordx4 v[40:43], v13, s[16:17] offset:3072
	s_add_u32 s22, s12, s22
	s_addc_u32 s23, s13, 0
	s_lshl_b64 s[10:11], s[8:9], 11
	s_add_u32 s10, s22, s10
	s_addc_u32 s11, s23, s11
	s_cmp_lt_i32 s3, 0x8000
	s_waitcnt vmcnt(3)
	v_bfe_u32 v18, v14, 16, 1
	v_bfe_u32 v19, v15, 16, 1
	v_bfe_u32 v21, v17, 16, 1
	v_bfe_u32 v20, v16, 16, 1
	v_add3_u32 v18, v14, v18, s20
	v_add3_u32 v14, v15, v19, s20
	v_add3_u32 v15, v17, v21, s20
	v_add3_u32 v19, v16, v20, s20
	v_and_b32_e32 v20, 0xffff0000, v14
	v_and_b32_e32 v21, 0xffff0000, v15
	v_or_b32_sdwa v14, v20, v18 dst_sel:DWORD dst_unused:UNUSED_PAD src0_sel:DWORD src1_sel:WORD_1
	v_or_b32_sdwa v15, v21, v19 dst_sel:DWORD dst_unused:UNUSED_PAD src0_sel:DWORD src1_sel:WORD_1
	global_store_dwordx2 v2, v[14:15], s[10:11]
	v_and_b32_e32 v18, 0xffff0000, v18
	v_and_b32_e32 v19, 0xffff0000, v19
	v_mul_f32_e32 v20, v20, v20
	v_mul_f32_e32 v21, v21, v21
	v_fmac_f32_e32 v20, v18, v18
	v_fmac_f32_e32 v21, v19, v19
	v_add_f32_e32 v18, v20, v21
	s_waitcnt vmcnt(3)
	v_mov_b64_e32 v[14:15], v[32:33]
	v_mov_b64_e32 v[16:17], v[34:35]
	v_bfe_u32 v22, v14, 16, 1
	v_bfe_u32 v23, v15, 16, 1
	v_bfe_u32 v25, v17, 16, 1
	v_bfe_u32 v24, v16, 16, 1
	v_add3_u32 v22, v14, v22, s20
	v_add3_u32 v14, v15, v23, s20
	v_add3_u32 v15, v17, v25, s20
	v_add3_u32 v23, v16, v24, s20
	v_and_b32_e32 v24, 0xffff0000, v14
	v_and_b32_e32 v25, 0xffff0000, v15
	v_or_b32_sdwa v14, v24, v22 dst_sel:DWORD dst_unused:UNUSED_PAD src0_sel:DWORD src1_sel:WORD_1
	v_or_b32_sdwa v15, v25, v23 dst_sel:DWORD dst_unused:UNUSED_PAD src0_sel:DWORD src1_sel:WORD_1
	global_store_dwordx2 v2, v[14:15], s[10:11] offset:512
	v_and_b32_e32 v19, 0xffff0000, v22
	v_and_b32_e32 v20, 0xffff0000, v23
	v_mul_f32_e32 v21, v24, v24
	v_mul_f32_e32 v22, v25, v25
	v_fmac_f32_e32 v21, v19, v19
	v_fmac_f32_e32 v22, v20, v20
	v_add_f32_e32 v19, v21, v22
	v_add_f32_e32 v18, v18, v19
	s_waitcnt vmcnt(3)
	v_mov_b64_e32 v[14:15], v[36:37]
	v_mov_b64_e32 v[16:17], v[38:39]
	v_bfe_u32 v26, v14, 16, 1
	v_bfe_u32 v27, v15, 16, 1
	v_bfe_u32 v29, v17, 16, 1
	v_bfe_u32 v28, v16, 16, 1
	v_add3_u32 v26, v14, v26, s20
	v_add3_u32 v14, v15, v27, s20
	v_add3_u32 v15, v17, v29, s20
	v_add3_u32 v27, v16, v28, s20
	v_and_b32_e32 v28, 0xffff0000, v14
	v_and_b32_e32 v29, 0xffff0000, v15
	v_or_b32_sdwa v14, v28, v26 dst_sel:DWORD dst_unused:UNUSED_PAD src0_sel:DWORD src1_sel:WORD_1
	v_or_b32_sdwa v15, v29, v27 dst_sel:DWORD dst_unused:UNUSED_PAD src0_sel:DWORD src1_sel:WORD_1
	global_store_dwordx2 v2, v[14:15], s[10:11] offset:1024
	v_and_b32_e32 v19, 0xffff0000, v26
	v_and_b32_e32 v20, 0xffff0000, v27
	v_mul_f32_e32 v21, v28, v28
	v_mul_f32_e32 v22, v29, v29
	v_fmac_f32_e32 v21, v19, v19
	v_fmac_f32_e32 v22, v20, v20
	v_add_f32_e32 v19, v21, v22
	v_add_f32_e32 v18, v18, v19
	s_waitcnt vmcnt(3)
	v_mov_b64_e32 v[14:15], v[40:41]
	v_mov_b64_e32 v[16:17], v[42:43]
	v_bfe_u32 v20, v15, 16, 1
	v_bfe_u32 v22, v17, 16, 1
	v_bfe_u32 v19, v14, 16, 1
	v_bfe_u32 v21, v16, 16, 1
	v_add3_u32 v15, v15, v20, s20
	v_add3_u32 v17, v17, v22, s20
	v_add3_u32 v14, v14, v19, s20
	v_add3_u32 v16, v16, v21, s20
	v_and_b32_e32 v15, 0xffff0000, v15
	v_and_b32_e32 v17, 0xffff0000, v17
	v_and_b32_e32 v19, 0xffff0000, v14
	v_and_b32_e32 v20, 0xffff0000, v16
	v_mul_f32_e32 v21, v15, v15
	v_mul_f32_e32 v22, v17, v17
	v_fmac_f32_e32 v21, v19, v19
	v_fmac_f32_e32 v22, v20, v20
	v_add_f32_e32 v19, v21, v22
	v_add_f32_e32 v18, v18, v19
	v_or_b32_sdwa v14, v15, v14 dst_sel:DWORD dst_unused:UNUSED_PAD src0_sel:DWORD src1_sel:WORD_1
	v_or_b32_sdwa v15, v17, v16 dst_sel:DWORD dst_unused:UNUSED_PAD src0_sel:DWORD src1_sel:WORD_1
	global_store_dwordx2 v2, v[14:15], s[10:11] offset:1536
	s_mov_b64 s[10:11], -1
	s_nop 1
	v_add_f32_dpp v18, v18, v18 quad_perm:[1,0,3,2] row_mask:0xf bank_mask:0xf
	s_nop 1
	v_add_f32_dpp v18, v18, v18 quad_perm:[2,3,0,1] row_mask:0xf bank_mask:0xf
	s_nop 1
	v_add_f32_dpp v18, v18, v18 row_half_mirror row_mask:0xf bank_mask:0xf
	s_nop 1
	v_add_f32_dpp v18, v18, v18 row_mirror row_mask:0xf bank_mask:0xf
	v_mov_b32_e32 v19, v18
	s_nop 1
	v_permlane16_swap_b32_e32 v19, v18
	v_add_f32_e32 v18, v18, v19
	v_mov_b32_e32 v19, v18
	s_nop 1
	v_permlane32_swap_b32_e32 v19, v18
	v_add_f32_e32 v14, v18, v19
	s_cbranch_scc1 .LBB0_357
	s_andn2_b64 vcc, exec, s[10:11]
	s_cbranch_vccnz .LBB0_354
	s_branch .LBB0_360
